# v28
# baseline (speedup 1.0000x reference)
.LBB1_30:
	s_endpgm
	s_nop 0
	s_nop 0
	s_nop 0
	s_nop 0
	s_nop 0
	s_nop 0
	s_endpgm
